# baseline (speedup 1.0000x reference)
.LBB0_8:
	s_load_dwordx4 s[4:7], s[0:1], 0x0
	v_and_b32_e32 v1, 63, v0
	s_cmpk_gt_i32 s12, 0xff
	s_mov_b64 s[2:3], -1
	s_cbranch_scc0 .LBB0_24
	v_and_b32_e32 v74, 31, v0
	v_lshrrev_b32_e32 v75, 5, v1
	v_lshrrev_b32_e32 v76, 6, v0
	s_lshl_b32 s8, s12, 2
	s_cmpk_gt_u32 s12, 0x1ff
	v_mov_b32_e32 v39, 0
	v_add_u32_e32 v77, s8, v76
	v_lshlrev_b32_e32 v36, 2, v74
	v_lshlrev_b32_e32 v34, 17, v75
	s_cbranch_scc0 .LBB0_11
	v_add_u32_e32 v4, 0xfffff800, v77
	s_load_dwordx2 s[2:3], s[0:1], 0x30
	v_lshrrev_b32_e32 v2, 2, v4
	v_and_b32_e32 v38, 0x3fffffc0, v2
	v_lshlrev_b64 v[2:3], 14, v[38:39]
	v_lshlrev_b32_e32 v4, 6, v4
	v_bfe_u32 v78, v0, 6, 1
	s_waitcnt lgkmcnt(0)
	v_and_b32_e32 v40, 0x3f80, v4
	v_mov_b32_e32 v41, v39
	v_lshlrev_b32_e32 v4, 8, v74
	v_lshl_add_u64 v[2:3], v[2:3], 0, v[40:41]
	v_mov_b32_e32 v37, v39
	v_lshl_or_b32 v4, v78, 13, v4
	v_mov_b32_e32 v5, v39
	v_lshl_add_u64 v[2:3], v[2:3], 0, v[36:37]
	v_lshl_add_u64 v[4:5], s[2:3], 0, v[4:5]
	v_lshlrev_b32_e32 v6, 5, v75
	v_mov_b32_e32 v7, v39
	v_mov_b32_e32 v35, v39
	v_lshl_add_u64 v[42:43], v[4:5], 0, v[6:7]
	v_lshl_add_u64 v[44:45], v[2:3], 0, v[34:35]
	s_movk_i32 s2, 0x4000
	global_load_dwordx4 v[26:29], v[42:43], off offset:16
	global_load_dwordx4 v[30:33], v[42:43], off
	global_load_dwordx4 v[18:21], v[42:43], off offset:80
	global_load_dwordx4 v[22:25], v[42:43], off offset:64
	global_load_dwordx4 v[10:13], v[42:43], off offset:144
	global_load_dwordx4 v[14:17], v[42:43], off offset:128
	global_load_dwordx4 v[2:5], v[42:43], off offset:208
	global_load_dwordx4 v[6:9], v[42:43], off offset:192
	v_add_u32_e32 v42, s2, v44
	s_mov_b32 s3, 0x8000
	v_add_u32_e32 v46, s3, v44
	s_mov_b32 s8, 0xc000
	v_add_u32_e32 v48, s8, v44
	s_mov_b32 s9, 0x10000
	v_add_u32_e32 v50, s9, v44
	s_mov_b32 s9, 0x14000
	v_add_u32_e32 v52, s9, v44
	s_mov_b32 s9, 0x18000
	v_add_u32_e32 v54, s9, v44
	s_mov_b32 s9, 0x1c000
	v_add_u32_e32 v56, s9, v44
	s_mov_b32 s9, 0x40000
	global_load_dword v72, v44, s[6:7]
	global_load_dword v73, v42, s[6:7]
	global_load_dword v70, v46, s[6:7]
	global_load_dword v71, v48, s[6:7]
	global_load_dword v68, v50, s[6:7]
	global_load_dword v69, v52, s[6:7]
	global_load_dword v66, v54, s[6:7]
	global_load_dword v67, v56, s[6:7]
	v_add_u32_e32 v42, s9, v44
	s_mov_b32 s10, 0x44000
	v_add_u32_e32 v46, s10, v44
	s_mov_b32 s11, 0x48000
	v_add_u32_e32 v48, s11, v44
	s_mov_b32 s13, 0x4c000
	v_add_u32_e32 v50, s13, v44
	s_mov_b32 s14, 0x50000
	v_add_u32_e32 v52, s14, v44
	s_mov_b32 s14, 0x54000
	v_add_u32_e32 v54, s14, v44
	s_mov_b32 s14, 0x58000
	v_add_u32_e32 v56, s14, v44
	s_mov_b32 s14, 0x5c000
	v_add_u32_e32 v80, s14, v44
	s_mov_b32 s14, 0x80000
	global_load_dword v64, v42, s[6:7]
	global_load_dword v65, v46, s[6:7]
	global_load_dword v62, v48, s[6:7]
	global_load_dword v63, v50, s[6:7]
	global_load_dword v60, v52, s[6:7]
	global_load_dword v61, v54, s[6:7]
	global_load_dword v58, v56, s[6:7]
	global_load_dword v59, v80, s[6:7]
	v_add_u32_e32 v42, s14, v44
	s_mov_b32 s14, 0x84000
	v_add_u32_e32 v46, s14, v44
	s_mov_b32 s14, 0x88000
	v_add_u32_e32 v48, s14, v44
	s_mov_b32 s14, 0x8c000
	v_add_u32_e32 v54, s14, v44
	s_mov_b32 s14, 0x90000
	v_add_u32_e32 v80, s14, v44
	s_mov_b32 s14, 0x94000
	v_add_u32_e32 v82, s14, v44
	s_mov_b32 s14, 0x98000
	global_load_dword v56, v42, s[6:7]
	global_load_dword v57, v46, s[6:7]
	global_load_dword v52, v48, s[6:7]
	global_load_dword v53, v54, s[6:7]
	global_load_dword v50, v80, s[6:7]
	global_load_dword v51, v82, s[6:7]
	v_add_u32_e32 v42, s14, v44
	s_mov_b32 s14, 0x9c000
	v_add_u32_e32 v46, s14, v44
	s_mov_b32 s14, 0xc0000
	global_load_dword v54, v42, s[6:7]
	global_load_dword v55, v46, s[6:7]
	v_add_u32_e32 v80, s14, v44
	s_mov_b32 s14, 0xc4000
	v_add_u32_e32 v82, s14, v44
	s_mov_b32 s14, 0xc8000
	v_add_u32_e32 v84, s14, v44
	s_mov_b32 s14, 0xcc000
	v_add_u32_e32 v86, s14, v44
	s_mov_b32 s14, 0xd0000
	v_add_u32_e32 v88, s14, v44
	s_mov_b32 s14, 0xd4000
	v_add_u32_e32 v90, s14, v44
	s_mov_b32 s14, 0xd8000
	v_add_u32_e32 v92, s14, v44
	s_mov_b32 s14, 0xdc000
	v_add_u32_e32 v94, s14, v44
	s_load_dwordx2 s[14:15], s[0:1], 0x58
	global_load_dword v48, v80, s[6:7]
	global_load_dword v49, v82, s[6:7]
	global_load_dword v46, v84, s[6:7]
	global_load_dword v47, v86, s[6:7]
	global_load_dword v44, v88, s[6:7]
	global_load_dword v45, v90, s[6:7]
	global_load_dword v42, v92, s[6:7]
	global_load_dword v43, v94, s[6:7]
	s_waitcnt vmcnt(38)
	s_waitcnt vmcnt(31)
	s_waitcnt vmcnt(30)
	s_waitcnt vmcnt(29)
	s_waitcnt vmcnt(28)
	s_waitcnt vmcnt(27)
	s_waitcnt vmcnt(26)
	s_waitcnt vmcnt(25)
	s_waitcnt vmcnt(24)
	s_waitcnt vmcnt(23)
	s_waitcnt vmcnt(22)
	s_waitcnt vmcnt(21)
	s_waitcnt vmcnt(20)
	s_waitcnt vmcnt(19)
	s_waitcnt vmcnt(18)
	s_waitcnt vmcnt(17)
	s_waitcnt vmcnt(16)
	v_cvt_pk_bf16_f32 v35, v72, 0
	v_cvt_pk_bf16_f32 v79, v73, 0
	v_lshlrev_b32_e32 v81, 16, v79
	v_lshlrev_b32_e32 v80, 16, v35
	v_pk_add_f32 v[82:83], v[72:73], v[80:81] neg_lo:[0,1] neg_hi:[0,1]
	v_cvt_pk_bf16_f32 v35, v70, 0
	v_cvt_pk_bf16_f32 v73, v71, 0
	v_lshlrev_b32_e32 v72, 16, v35
	v_lshlrev_b32_e32 v73, 16, v73
	v_pk_add_f32 v[84:85], v[70:71], v[72:73] neg_lo:[0,1] neg_hi:[0,1]
	v_cvt_pk_bf16_f32 v35, v68, 0
	v_cvt_pk_bf16_f32 v70, v69, 0
	v_lshlrev_b32_e32 v86, 16, v35
	v_lshlrev_b32_e32 v87, 16, v70
	v_pk_add_f32 v[88:89], v[68:69], v[86:87] neg_lo:[0,1] neg_hi:[0,1]
	v_cvt_pk_bf16_f32 v35, v66, 0
	v_cvt_pk_bf16_f32 v68, v67, 0
	v_lshlrev_b32_e32 v90, 16, v35
	v_lshlrev_b32_e32 v91, 16, v68
	v_pk_add_f32 v[92:93], v[66:67], v[90:91] neg_lo:[0,1] neg_hi:[0,1]
	v_cvt_pk_bf16_f32 v35, v30, 0
	v_cvt_pk_bf16_f32 v66, v31, 0
	v_cvt_pk_bf16_f32 v68, v26, 0
	v_lshlrev_b32_e32 v67, 16, v66
	v_lshlrev_b32_e32 v66, 16, v35
	v_cvt_pk_bf16_f32 v35, v27, 0
	v_lshlrev_b32_e32 v69, 16, v35
	v_lshlrev_b32_e32 v68, 16, v68
	v_pk_add_f32 v[94:95], v[26:27], v[68:69] neg_lo:[0,1] neg_hi:[0,1]
	v_cvt_pk_bf16_f32 v26, v32, 0
	v_cvt_pk_bf16_f32 v35, v28, 0
	v_cvt_pk_bf16_f32 v27, v33, 0
	v_cvt_pk_bf16_f32 v70, v29, 0
	v_lshlrev_b32_e32 v26, 16, v26
	v_lshlrev_b32_e32 v27, 16, v27
	v_lshlrev_b32_e32 v96, 16, v35
	v_lshlrev_b32_e32 v97, 16, v70
	v_pk_add_f32 v[30:31], v[30:31], v[66:67] neg_lo:[0,1] neg_hi:[0,1]
	v_cvt_pk_bf16_f32 v66, v66, v67
	v_cvt_pk_bf16_f32 v67, v26, v27
	v_cvt_pk_bf16_f32 v68, v68, v69
	v_cvt_pk_bf16_f32 v69, v96, v97
	v_cvt_pk_bf16_f32 v70, v80, v81
	v_cvt_pk_bf16_f32 v71, v72, v73
	v_cvt_pk_bf16_f32 v72, v86, v87
	v_cvt_pk_bf16_f32 v73, v90, v91
	v_pk_add_f32 v[32:33], v[32:33], v[26:27] neg_lo:[0,1] neg_hi:[0,1]
	v_pk_add_f32 v[80:81], v[28:29], v[96:97] neg_lo:[0,1] neg_hi:[0,1]
	v_mfma_f32_32x32x16_bf16 a[0:15], v[66:69], v[70:73], 0
	v_cvt_pk_bf16_f32 v26, v82, v83
	v_cvt_pk_bf16_f32 v27, v84, v85
	v_cvt_pk_bf16_f32 v28, v88, v89
	v_cvt_pk_bf16_f32 v29, v92, v93
	v_cvt_pk_bf16_f32 v30, v30, v31
	v_cvt_pk_bf16_f32 v31, v32, v33
	v_cvt_pk_bf16_f32 v32, v94, v95
	v_mfma_f32_32x32x16_bf16 a[0:15], v[66:69], v[26:29], a[0:15]
	v_cvt_pk_bf16_f32 v33, v80, v81
	v_cvt_pk_bf16_f32 v26, v64, 0
	v_cvt_pk_bf16_f32 v27, v65, 0
	v_cvt_pk_bf16_f32 v28, v18, 0
	v_cvt_pk_bf16_f32 v29, v19, 0
	v_lshlrev_b32_e32 v29, 16, v29
	v_lshlrev_b32_e32 v28, 16, v28
	v_mfma_f32_32x32x16_bf16 a[0:15], v[30:33], v[70:73], a[0:15]
	v_lshlrev_b32_e32 v30, 16, v26
	v_lshlrev_b32_e32 v31, 16, v27
	v_cvt_pk_bf16_f32 v26, v62, 0
	v_cvt_pk_bf16_f32 v27, v63, 0
	v_lshlrev_b32_e32 v32, 16, v26
	v_lshlrev_b32_e32 v33, 16, v27
	v_cvt_pk_bf16_f32 v26, v60, 0
	v_cvt_pk_bf16_f32 v27, v61, 0
	v_lshlrev_b32_e32 v66, 16, v26
	v_lshlrev_b32_e32 v67, 16, v27
	v_cvt_pk_bf16_f32 v26, v58, 0
	v_cvt_pk_bf16_f32 v27, v59, 0
	v_lshlrev_b32_e32 v68, 16, v26
	v_lshlrev_b32_e32 v69, 16, v27
	v_cvt_pk_bf16_f32 v26, v22, 0
	v_cvt_pk_bf16_f32 v27, v23, 0
	v_pk_add_f32 v[70:71], v[18:19], v[28:29] neg_lo:[0,1] neg_hi:[0,1]
	v_cvt_pk_bf16_f32 v18, v24, 0
	v_cvt_pk_bf16_f32 v35, v20, 0
	v_cvt_pk_bf16_f32 v19, v25, 0
	v_cvt_pk_bf16_f32 v73, v21, 0
	v_lshlrev_b32_e32 v27, 16, v27
	v_lshlrev_b32_e32 v26, 16, v26
	v_lshlrev_b32_e32 v18, 16, v18
	v_lshlrev_b32_e32 v19, 16, v19
	v_lshlrev_b32_e32 v72, 16, v35
	v_lshlrev_b32_e32 v73, 16, v73
	v_pk_add_f32 v[22:23], v[22:23], v[26:27] neg_lo:[0,1] neg_hi:[0,1]
	v_cvt_pk_bf16_f32 v26, v26, v27
	v_cvt_pk_bf16_f32 v27, v18, v19
	v_cvt_pk_bf16_f32 v28, v28, v29
	v_cvt_pk_bf16_f32 v29, v72, v73
	v_pk_add_f32 v[64:65], v[64:65], v[30:31] neg_lo:[0,1] neg_hi:[0,1]
	v_pk_add_f32 v[62:63], v[62:63], v[32:33] neg_lo:[0,1] neg_hi:[0,1]
	v_cvt_pk_bf16_f32 v30, v30, v31
	v_cvt_pk_bf16_f32 v31, v32, v33
	v_cvt_pk_bf16_f32 v32, v66, v67
	v_cvt_pk_bf16_f32 v33, v68, v69
	v_pk_add_f32 v[60:61], v[60:61], v[66:67] neg_lo:[0,1] neg_hi:[0,1]
	v_pk_add_f32 v[58:59], v[58:59], v[68:69] neg_lo:[0,1] neg_hi:[0,1]
	v_mfma_f32_32x32x16_bf16 a[0:15], v[26:29], v[30:33], a[0:15]
	v_add_f32_e64 v24, v24, -v18
	v_add_f32_e64 v25, v25, -v19
	v_add_f32_e64 v66, v20, -v72
	v_add_f32_e64 v67, v21, -v73
	v_cvt_pk_bf16_f32 v18, v64, v65
	v_cvt_pk_bf16_f32 v19, v62, v63
	v_cvt_pk_bf16_f32 v20, v60, v61
	v_cvt_pk_bf16_f32 v21, v58, v59
	v_cvt_pk_bf16_f32 v22, v22, v23
	v_cvt_pk_bf16_f32 v23, v24, v25
	v_mfma_f32_32x32x16_bf16 a[0:15], v[26:29], v[18:21], a[0:15]
	v_cvt_pk_bf16_f32 v24, v70, v71
	v_cvt_pk_bf16_f32 v25, v66, v67
	s_waitcnt vmcnt(15)
	s_waitcnt vmcnt(14)
	s_waitcnt vmcnt(13)
	s_waitcnt vmcnt(12)
	s_waitcnt vmcnt(11)
	s_waitcnt vmcnt(10)
	s_waitcnt vmcnt(9)
	s_waitcnt vmcnt(8)
	v_cvt_pk_bf16_f32 v20, v10, 0
	v_cvt_pk_bf16_f32 v18, v56, 0
	v_cvt_pk_bf16_f32 v19, v57, 0
	v_mfma_f32_32x32x16_bf16 a[0:15], v[22:25], v[30:33], a[0:15]
	v_lshlrev_b32_e32 v22, 16, v18
	v_lshlrev_b32_e32 v23, 16, v19
	v_cvt_pk_bf16_f32 v18, v52, 0
	v_cvt_pk_bf16_f32 v19, v53, 0
	v_lshlrev_b32_e32 v24, 16, v18
	v_lshlrev_b32_e32 v25, 16, v19
	v_cvt_pk_bf16_f32 v18, v50, 0
	v_cvt_pk_bf16_f32 v19, v51, 0
	v_lshlrev_b32_e32 v30, 16, v18
	v_lshlrev_b32_e32 v31, 16, v19
	v_cvt_pk_bf16_f32 v18, v54, 0
	v_cvt_pk_bf16_f32 v19, v55, 0
	v_cvt_pk_bf16_f32 v21, v11, 0
	v_pk_add_f32 v[32:33], v[50:51], v[30:31] neg_lo:[0,1] neg_hi:[0,1]
	v_lshlrev_b32_e32 v50, 16, v18
	v_lshlrev_b32_e32 v51, 16, v19
	v_lshlrev_b32_e32 v21, 16, v21
	v_lshlrev_b32_e32 v20, 16, v20
	v_pk_add_f32 v[26:27], v[56:57], v[22:23] neg_lo:[0,1] neg_hi:[0,1]
	v_pk_add_f32 v[28:29], v[52:53], v[24:25] neg_lo:[0,1] neg_hi:[0,1]
	v_pk_add_f32 v[52:53], v[54:55], v[50:51] neg_lo:[0,1] neg_hi:[0,1]
	v_cvt_pk_bf16_f32 v18, v14, 0
	v_cvt_pk_bf16_f32 v19, v15, 0
	v_pk_add_f32 v[54:55], v[10:11], v[20:21] neg_lo:[0,1] neg_hi:[0,1]
	v_cvt_pk_bf16_f32 v10, v16, 0
	v_cvt_pk_bf16_f32 v35, v12, 0
	v_cvt_pk_bf16_f32 v11, v17, 0
	v_cvt_pk_bf16_f32 v57, v13, 0
	v_lshlrev_b32_e32 v19, 16, v19
	v_lshlrev_b32_e32 v18, 16, v18
	v_lshlrev_b32_e32 v10, 16, v10
	v_lshlrev_b32_e32 v11, 16, v11
	v_lshlrev_b32_e32 v56, 16, v35
	v_lshlrev_b32_e32 v57, 16, v57
	v_pk_add_f32 v[14:15], v[14:15], v[18:19] neg_lo:[0,1] neg_hi:[0,1]
	v_cvt_pk_bf16_f32 v18, v18, v19
	v_cvt_pk_bf16_f32 v19, v10, v11
	v_cvt_pk_bf16_f32 v20, v20, v21
	v_cvt_pk_bf16_f32 v21, v56, v57
	v_cvt_pk_bf16_f32 v22, v22, v23
	v_cvt_pk_bf16_f32 v23, v24, v25
	v_cvt_pk_bf16_f32 v24, v30, v31
	v_cvt_pk_bf16_f32 v25, v50, v51
	v_pk_add_f32 v[16:17], v[16:17], v[10:11] neg_lo:[0,1] neg_hi:[0,1]
	v_pk_add_f32 v[30:31], v[12:13], v[56:57] neg_lo:[0,1] neg_hi:[0,1]
	v_mfma_f32_32x32x16_bf16 a[0:15], v[18:21], v[22:25], a[0:15]
	v_cvt_pk_bf16_f32 v10, v26, v27
	v_cvt_pk_bf16_f32 v11, v28, v29
	v_cvt_pk_bf16_f32 v12, v32, v33
	v_cvt_pk_bf16_f32 v13, v52, v53
	v_cvt_pk_bf16_f32 v14, v14, v15
	v_cvt_pk_bf16_f32 v15, v16, v17
	v_cvt_pk_bf16_f32 v16, v54, v55
	v_mfma_f32_32x32x16_bf16 a[0:15], v[18:21], v[10:13], a[0:15]
	v_cvt_pk_bf16_f32 v17, v30, v31
	s_waitcnt vmcnt(7)
	s_waitcnt vmcnt(6)
	s_waitcnt vmcnt(5)
	s_waitcnt vmcnt(4)
	s_waitcnt vmcnt(3)
	s_waitcnt vmcnt(2)
	s_waitcnt vmcnt(1)
	s_waitcnt vmcnt(0)
	v_lshl_or_b32 v38, v78, 5, v38
	v_cvt_pk_bf16_f32 v10, v48, 0
	v_cvt_pk_bf16_f32 v11, v49, 0
	v_mfma_f32_32x32x16_bf16 a[0:15], v[14:17], v[22:25], a[0:15]
	v_lshlrev_b32_e32 v14, 16, v10
	v_lshlrev_b32_e32 v15, 16, v11
	v_cvt_pk_bf16_f32 v10, v46, 0
	v_cvt_pk_bf16_f32 v11, v47, 0
	v_lshlrev_b32_e32 v16, 16, v10
	v_lshlrev_b32_e32 v17, 16, v11
	v_cvt_pk_bf16_f32 v10, v44, 0
	v_cvt_pk_bf16_f32 v11, v45, 0
	v_cvt_pk_bf16_f32 v12, v2, 0
	v_cvt_pk_bf16_f32 v13, v3, 0
	v_lshlrev_b32_e32 v22, 16, v10
	v_lshlrev_b32_e32 v23, 16, v11
	v_cvt_pk_bf16_f32 v10, v42, 0
	v_cvt_pk_bf16_f32 v11, v43, 0
	v_lshlrev_b32_e32 v13, 16, v13
	v_lshlrev_b32_e32 v12, 16, v12
	v_lshlrev_b32_e32 v26, 16, v10
	v_lshlrev_b32_e32 v27, 16, v11
	v_cvt_pk_bf16_f32 v10, v6, 0
	v_cvt_pk_bf16_f32 v11, v7, 0
	v_pk_add_f32 v[30:31], v[2:3], v[12:13] neg_lo:[0,1] neg_hi:[0,1]
	v_cvt_pk_bf16_f32 v2, v8, 0
	v_cvt_pk_bf16_f32 v32, v4, 0
	v_cvt_pk_bf16_f32 v3, v9, 0
	v_cvt_pk_bf16_f32 v33, v5, 0
	v_lshlrev_b32_e32 v11, 16, v11
	v_lshlrev_b32_e32 v10, 16, v10
	v_lshlrev_b32_e32 v2, 16, v2
	v_lshlrev_b32_e32 v3, 16, v3
	v_lshlrev_b32_e32 v32, 16, v32
	v_lshlrev_b32_e32 v33, 16, v33
	v_pk_add_f32 v[6:7], v[6:7], v[10:11] neg_lo:[0,1] neg_hi:[0,1]
	v_cvt_pk_bf16_f32 v10, v10, v11
	v_cvt_pk_bf16_f32 v11, v2, v3
	v_cvt_pk_bf16_f32 v12, v12, v13
	v_cvt_pk_bf16_f32 v13, v32, v33
	v_pk_add_f32 v[18:19], v[48:49], v[14:15] neg_lo:[0,1] neg_hi:[0,1]
	v_pk_add_f32 v[20:21], v[46:47], v[16:17] neg_lo:[0,1] neg_hi:[0,1]
	v_cvt_pk_bf16_f32 v14, v14, v15
	v_cvt_pk_bf16_f32 v15, v16, v17
	v_cvt_pk_bf16_f32 v16, v22, v23
	v_cvt_pk_bf16_f32 v17, v26, v27
	v_pk_add_f32 v[24:25], v[44:45], v[22:23] neg_lo:[0,1] neg_hi:[0,1]
	v_pk_add_f32 v[28:29], v[42:43], v[26:27] neg_lo:[0,1] neg_hi:[0,1]
	v_mfma_f32_32x32x16_bf16 a[0:15], v[10:13], v[14:17], a[0:15]
	v_add_f32_e64 v8, v8, -v2
	v_add_f32_e64 v9, v9, -v3
	v_add_f32_e64 v22, v4, -v32
	v_add_f32_e64 v23, v5, -v33
	v_cvt_pk_bf16_f32 v2, v18, v19
	v_cvt_pk_bf16_f32 v3, v20, v21
	v_cvt_pk_bf16_f32 v4, v24, v25
	v_cvt_pk_bf16_f32 v5, v28, v29
	v_cvt_pk_bf16_f32 v6, v6, v7
	v_cvt_pk_bf16_f32 v7, v8, v9
	v_mfma_f32_32x32x16_bf16 a[0:15], v[10:13], v[2:5], a[0:15]
	v_cvt_pk_bf16_f32 v8, v30, v31
	v_cvt_pk_bf16_f32 v9, v22, v23
	v_lshrrev_b32_e32 v38, 6, v0
	s_lshl_b32 s2, s12, 2
	s_add_i32 s2, s2, 0xfffff800
	v_add_u32_e32 v38, s2, v38
	v_lshlrev_b32_e32 v38, 12, v38
	v_lshl_add_u32 v38, v1, 4, v38
	s_waitcnt lgkmcnt(0)
	v_mfma_f32_32x32x16_bf16 a[0:15], v[6:9], v[14:17], a[0:15]
	s_mov_b64 s[2:3], 0
	s_nop 7
	s_nop 4
	global_store_dwordx4 v38, a[0:3], s[14:15] sc1
	global_store_dwordx4 v38, a[4:7], s[14:15] offset:1024 sc1
	global_store_dwordx4 v38, a[8:11], s[14:15] offset:2048 sc1
	global_store_dwordx4 v38, a[12:15], s[14:15] offset:3072 sc1
.LBB0_11:
	s_andn2_b64 vcc, exec, s[2:3]
	s_cbranch_vccnz .LBB0_23
	v_add_u32_e32 v18, 0xfffffc00, v77
	v_lshrrev_b32_e32 v2, 3, v18
	v_and_b32_e32 v20, 0x1fffffc0, v2
	v_mov_b32_e32 v21, 0
	v_lshlrev_b64 v[2:3], 14, v[20:21]
	v_lshlrev_b32_e32 v4, 7, v18
	s_waitcnt lgkmcnt(0)
	v_and_b32_e32 v20, 0x3f80, v4
	v_lshl_add_u64 v[2:3], v[2:3], 0, v[20:21]
	v_mov_b32_e32 v37, v21
	v_lshl_add_u64 v[2:3], v[2:3], 0, v[36:37]
	v_mov_b32_e32 v35, v21
	v_lshl_add_u64 v[2:3], v[2:3], 0, v[34:35]
	s_movk_i32 s10, 0x4000
	v_add_u32_e32 v4, s10, v2
	s_mov_b32 s10, 0x8000
	v_add_u32_e32 v6, s10, v2
	s_mov_b32 s10, 0xc000
	v_add_u32_e32 v8, s10, v2
	s_mov_b32 s10, 0x10000
	v_add_u32_e32 v10, s10, v2
	s_mov_b32 s10, 0x14000
	v_add_u32_e32 v12, s10, v2
	s_mov_b32 s10, 0x18000
	v_add_u32_e32 v14, s10, v2
	s_mov_b32 s10, 0x1c000
	v_add_u32_e32 v16, s10, v2
	s_mov_b32 s10, 0x40000
	s_load_dwordx2 s[2:3], s[0:1], 0x20
	s_load_dwordx2 s[8:9], s[0:1], 0x10
	s_load_dwordx2 s[14:15], s[0:1], 0x28
	s_load_dwordx2 s[16:17], s[0:1], 0x18
	global_load_dword v44, v2, s[4:5]
	global_load_dword v43, v4, s[4:5]
	global_load_dword v42, v6, s[4:5]
	global_load_dword v41, v8, s[4:5]
	global_load_dword v40, v10, s[4:5]
	global_load_dword v38, v12, s[4:5]
	global_load_dword v19, v14, s[4:5]
	global_load_dword v39, v16, s[4:5]
	v_add_u32_e32 v4, s10, v2
	s_mov_b32 s10, 0x44000
	v_add_u32_e32 v6, s10, v2
	s_mov_b32 s10, 0x48000
	v_add_u32_e32 v8, s10, v2
	s_mov_b32 s10, 0x4c000
	v_add_u32_e32 v10, s10, v2
	s_mov_b32 s10, 0x50000
	v_add_u32_e32 v12, s10, v2
	s_mov_b32 s10, 0x54000
	v_add_u32_e32 v14, s10, v2
	s_mov_b32 s10, 0x58000
	v_add_u32_e32 v16, s10, v2
	s_mov_b32 s10, 0x5c000
	v_add_u32_e32 v22, s10, v2
	s_mov_b32 s10, 0x80000
	global_load_dword v52, v4, s[4:5]
	global_load_dword v51, v6, s[4:5]
	global_load_dword v50, v8, s[4:5]
	global_load_dword v49, v10, s[4:5]
	global_load_dword v48, v12, s[4:5]
	global_load_dword v46, v14, s[4:5]
	global_load_dword v45, v16, s[4:5]
	global_load_dword v47, v22, s[4:5]
	v_add_u32_e32 v4, s10, v2
	s_mov_b32 s10, 0x84000
	v_add_u32_e32 v6, s10, v2
	s_mov_b32 s10, 0x88000
	v_add_u32_e32 v8, s10, v2
	s_mov_b32 s10, 0x8c000
	v_add_u32_e32 v10, s10, v2
	s_mov_b32 s10, 0x90000
	v_add_u32_e32 v12, s10, v2
	s_mov_b32 s10, 0x94000
	v_add_u32_e32 v14, s10, v2
	s_mov_b32 s10, 0x98000
	v_add_u32_e32 v16, s10, v2
	s_mov_b32 s10, 0x9c000
	v_add_u32_e32 v22, s10, v2
	s_mov_b32 s10, 0xc0000
	global_load_dword v60, v4, s[4:5]
	global_load_dword v59, v6, s[4:5]
	global_load_dword v58, v8, s[4:5]
	global_load_dword v57, v10, s[4:5]
	global_load_dword v56, v12, s[4:5]
	global_load_dword v54, v14, s[4:5]
	global_load_dword v53, v16, s[4:5]
	global_load_dword v55, v22, s[4:5]
	v_add_u32_e32 v4, s10, v2
	s_mov_b32 s10, 0xc4000
	v_add_u32_e32 v6, s10, v2
	s_mov_b32 s10, 0xc8000
	v_add_u32_e32 v8, s10, v2
	s_mov_b32 s10, 0xcc000
	v_add_u32_e32 v10, s10, v2
	s_mov_b32 s10, 0xd0000
	v_add_u32_e32 v12, s10, v2
	s_mov_b32 s10, 0xd4000
	v_add_u32_e32 v14, s10, v2
	s_mov_b32 s10, 0xd8000
	v_add_u32_e32 v16, s10, v2
	s_mov_b32 s10, 0xdc000
	v_add_u32_e32 v2, s10, v2
	v_bfe_u32 v69, v18, 7, 2
	v_lshlrev_b32_e32 v20, 14, v69
	global_load_dword v68, v4, s[4:5]
	global_load_dword v67, v6, s[4:5]
	global_load_dword v66, v8, s[4:5]
	global_load_dword v65, v10, s[4:5]
	global_load_dword v64, v12, s[4:5]
	global_load_dword v62, v14, s[4:5]
	global_load_dword v61, v16, s[4:5]
	global_load_dword v63, v2, s[4:5]
	s_waitcnt lgkmcnt(0)
	v_lshl_add_u64 v[2:3], s[8:9], 0, v[20:21]
	v_lshlrev_b32_e32 v20, 4, v0
	v_lshlrev_b32_e32 v4, 12, v69
	v_lshl_add_u64 v[70:71], v[2:3], 0, v[20:21]
	s_movk_i32 s8, 0x2000
	v_add_co_u32_e32 v72, vcc, s8, v70
	v_lshl_or_b32 v2, v76, 10, v4
	s_nop 0
	v_addc_co_u32_e32 v73, vcc, 0, v71, vcc
	s_movk_i32 s8, 0x3000
	v_or_b32_e32 v3, v2, v1
	v_add_co_u32_e32 v78, vcc, s8, v70
	v_lshlrev_b32_e32 v77, 2, v3
	v_or_b32_e32 v2, v2, v0
	v_mov_b32_e32 v3, 0xf00
	v_addc_co_u32_e32 v79, vcc, 0, v71, vcc
	global_load_dword v26, v77, s[2:3]
	global_load_dword v27, v77, s[2:3] offset:256
	global_load_dword v28, v77, s[2:3] offset:512
	global_load_dword v29, v77, s[2:3] offset:768
	global_load_dword v22, v77, s[2:3] offset:1024
	global_load_dword v23, v77, s[2:3] offset:1280
	global_load_dword v24, v77, s[2:3] offset:1536
	global_load_dword v25, v77, s[2:3] offset:1792
	v_lshl_or_b32 v80, v2, 2, v3
	global_load_dword v34, v77, s[2:3] offset:2048
	global_load_dword v35, v77, s[2:3] offset:2304
	global_load_dword v36, v77, s[2:3] offset:2560
	global_load_dword v37, v77, s[2:3] offset:2816
	global_load_dword v30, v77, s[2:3] offset:3072
	global_load_dword v31, v77, s[2:3] offset:3328
	global_load_dword v32, v77, s[2:3] offset:3584
	global_load_dword v33, v80, s[2:3]
	global_load_dwordx4 v[10:13], v[72:73], off offset:-4096
	global_load_dwordx4 v[6:9], v[72:73], off
	global_load_dwordx4 v[14:17], v[70:71], off
	global_load_dwordx4 v[2:5], v[78:79], off
	s_load_dwordx2 s[8:9], s[0:1], 0x48
	s_load_dwordx2 s[26:27], s[0:1], 0x50
	s_load_dwordx2 s[28:29], s[0:1], 0x60
	s_load_dwordx2 s[30:31], s[0:1], 0x68
	v_cmp_gt_u32_e32 vcc, 32, v0
	v_mov_b32_e32 v71, v21
	v_mov_b32_e32 v72, v21
	v_mov_b32_e32 v73, v21
	s_and_saveexec_b64 s[10:11], vcc
	s_cbranch_execz .LBB0_14
	v_cmp_gt_u32_e64 s[2:3], 16, v0
	v_lshlrev_b32_e32 v21, 2, v0
	v_lshlrev_b32_e32 v69, 6, v69
	v_mov_b32_e32 v70, s15
	v_mov_b32_e32 v71, s17
	v_cndmask_b32_e64 v71, v70, v71, s[2:3]
	v_mov_b32_e32 v70, s14
	v_mov_b32_e32 v72, s16
	v_cndmask_b32_e64 v70, v70, v72, s[2:3]
	v_lshlrev_b32_e32 v72, 2, v69
	v_mov_b32_e32 v73, 0
	v_and_b32_e32 v21, 60, v21
	v_lshl_add_u64 v[70:71], v[70:71], 0, v[72:73]
	v_lshlrev_b32_e32 v72, 2, v21
	v_lshl_add_u64 v[70:71], v[70:71], 0, v[72:73]
	global_load_dwordx4 v[70:73], v[70:71], off
	s_waitcnt vmcnt(0)
	v_mov_b32_e32 v21, v70
